# speedup vs baseline: 1.0174x; 1.0079x over previous
.Lk1p_o:
	s_mov_b64 exec, s[8:9]
	ds_read_b32 v16, v16
	ds_read_b32 v17, v17
	ds_read_b32 v18, v18
	ds_read_b32 v19, v19
	s_waitcnt lgkmcnt(0)
	v_add_u32_e32 v4, v16, v48
	v_lshlrev_b32_e32 v4, 2, v4
	ds_write_b32 v4, v32 offset:4352
	v_add_u32_e32 v5, v17, v49
	v_lshlrev_b32_e32 v5, 2, v5
	ds_write_b32 v5, v33 offset:4352
	v_add_u32_e32 v6, v18, v50
	v_lshlrev_b32_e32 v6, 2, v6
	ds_write_b32 v6, v34 offset:4352
	v_add_u32_e32 v7, v19, v51
	v_lshlrev_b32_e32 v7, 2, v7
	ds_write_b32 v7, v35 offset:4352
	s_waitcnt lgkmcnt(0)
	s_barrier
	s_sub_u32 s16, 0xf4240, s3
	s_min_u32 s16, s16, 0x1000
	s_lshl_b32 s17, s3, 2
	v_add_u32_e32 v6, s17, v1
	ds_read_b32 v16, v1 offset:4352
	ds_read_b32 v17, v1 offset:8448
	ds_read_b32 v18, v1 offset:12544
	ds_read_b32 v19, v1 offset:16640
	v_add_u32_e32 v7, 0x400, v0
	v_add_u32_e32 v8, 0x800, v0
	v_add_u32_e32 v9, 0xc00, v0
	v_cmp_gt_u32_e32 vcc, s16, v0
	v_cmp_gt_u32_e64 s[8:9], s16, v7
	v_cmp_gt_u32_e64 s[10:11], s16, v8
	v_cmp_gt_u32_e64 s[18:19], s16, v9
	v_add_u32_e32 v7, 0x1000, v6
	v_add_u32_e32 v8, 0x2000, v6
	v_add_u32_e32 v9, 0x3000, v6
	s_waitcnt lgkmcnt(0)
	s_mov_b64 exec, vcc
	s_cbranch_execz .LBB0_98
	global_store_dword v6, v16, s[12:13] sc1
	s_mov_b64 exec, s[8:9]
	s_cbranch_execz .LBB0_98
	global_store_dword v7, v17, s[12:13] sc1
	s_mov_b64 exec, s[10:11]
	s_cbranch_execz .LBB0_98
	global_store_dword v8, v18, s[12:13] sc1
	s_mov_b64 exec, s[18:19]
	s_cbranch_execz .LBB0_98
	global_store_dword v9, v19, s[12:13] sc1
